# speedup vs baseline: 1.0282x; 1.0282x over previous
_Z2kA5AArgs:
	s_load_dwordx2 s[34:35], s[0:1], 0x20
	s_load_dwordx16 s[16:31], s[0:1], 0x30
	s_lshl_b32 s3, s2, 3
	v_readfirstlane_b32 s38, v0
	s_and_b32 s3, s3, 56
	s_ashr_i32 s4, s2, 5
	s_lshr_b32 s36, s38, 6
	s_add_i32 s3, s3, s4
	s_bfe_u32 s33, s2, 0x20003
	s_cmp_lt_u32 s33, 1
	s_cbranch_scc1 .Lstag_done
	s_sleep 5
	s_cmp_lt_u32 s33, 2
	s_cbranch_scc1 .Lstag_done
	s_sleep 5
	s_cmp_lt_u32 s33, 3
	s_cbranch_scc1 .Lstag_done
	s_sleep 5
.Lstag_done:
	v_and_b32_e32 v1, 63, v0
	s_cmpk_gt_u32 s38, 0xff
	s_mov_b64 s[4:5], -1
	s_cbranch_scc1 .LBB0_3
	s_andn2_b64 vcc, exec, s[4:5]
	s_cbranch_vccz .LBB0_78
